# nt on the adaLN weight loads and on the finish-phase row loads (read-once streams)
# baseline (speedup 1.0000x reference)
.LBB0_15:
	s_mul_hi_i32 s4, s14, 0x2aaaaaab
	s_lshr_b32 s5, s4, 31
	s_ashr_i32 s4, s4, 3
	s_add_i32 s4, s4, s5
	s_mul_i32 s5, s4, 48
	s_sub_i32 s5, s14, s5
	v_lshl_or_b32 v6, s5, 7, v18
	s_ashr_i32 s5, s4, 31
	s_lshl_b64 s[6:7], s[4:5], 10
	v_lshl_add_u64 v[8:9], s[6:7], 0, v[2:3]
	v_mad_u64_u32 v[10:11], s[6:7], v8, s8, v[4:5]
	v_mad_i32_i24 v11, v9, s8, v11
	v_ashrrev_i32_e32 v7, 31, v6
	v_lshl_add_u64 v[8:9], v[6:7], 2, v[10:11]
	v_mov_b32_e32 v10, 0
	s_mov_b64 s[6:7], 0
	v_mov_b32_e32 v22, v19
	v_mov_b32_e32 v11, v10
	v_mov_b32_e32 v12, v10
	v_mov_b32_e32 v13, v10
	v_mov_b32_e32 v14, v10
	v_mov_b32_e32 v15, v10
	v_mov_b32_e32 v16, v10
	v_mov_b32_e32 v17, v10
	v_mov_b32_e32 v23, v10
	v_readfirstlane_b32 s100, v8
	v_readfirstlane_b32 s101, v9
	v_and_b32_e32 v200, 63, v0
	v_lshlrev_b32_e32 v200, 2, v200
	s_nop 4
	global_load_dword v70, v200, s[100:101] nt
	s_add_u32 s100, s100, 0x6000
	s_addc_u32 s101, s101, 0
	global_load_dword v72, v200, s[100:101] nt
	s_add_u32 s100, s100, 0x6000
	s_addc_u32 s101, s101, 0
	global_load_dword v74, v200, s[100:101] nt
	s_add_u32 s100, s100, 0x6000
	s_addc_u32 s101, s101, 0
	global_load_dword v76, v200, s[100:101] nt
	s_add_u32 s100, s100, 0x6000
	s_addc_u32 s101, s101, 0
	global_load_dword v78, v200, s[100:101] nt
	s_add_u32 s100, s100, 0x6000
	s_addc_u32 s101, s101, 0
	global_load_dword v80, v200, s[100:101] nt
	s_add_u32 s100, s100, 0x6000
	s_addc_u32 s101, s101, 0
	global_load_dword v82, v200, s[100:101] nt
	s_add_u32 s100, s100, 0x6000
	s_addc_u32 s101, s101, 0
	global_load_dword v84, v200, s[100:101] nt
	s_add_u32 s100, s100, 0x6000
	s_addc_u32 s101, s101, 0
	global_load_dword v86, v200, s[100:101] nt
	s_add_u32 s100, s100, 0x6000
	s_addc_u32 s101, s101, 0
	global_load_dword v88, v200, s[100:101] nt
	s_add_u32 s100, s100, 0x6000
	s_addc_u32 s101, s101, 0
	global_load_dword v90, v200, s[100:101] nt
	s_add_u32 s100, s100, 0x6000
	s_addc_u32 s101, s101, 0
	global_load_dword v92, v200, s[100:101] nt
	s_add_u32 s100, s100, 0x6000
	s_addc_u32 s101, s101, 0
	global_load_dword v94, v200, s[100:101] nt
	s_add_u32 s100, s100, 0x6000
	s_addc_u32 s101, s101, 0
	global_load_dword v96, v200, s[100:101] nt
	s_add_u32 s100, s100, 0x6000
	s_addc_u32 s101, s101, 0
	global_load_dword v98, v200, s[100:101] nt
	s_add_u32 s100, s100, 0x6000
	s_addc_u32 s101, s101, 0
	global_load_dword v100, v200, s[100:101] nt
	s_add_u32 s100, s100, 0x6000
	s_addc_u32 s101, s101, 0
	global_load_dword v102, v200, s[100:101] nt
	s_add_u32 s100, s100, 0x6000
	s_addc_u32 s101, s101, 0
	global_load_dword v104, v200, s[100:101] nt
	s_add_u32 s100, s100, 0x6000
	s_addc_u32 s101, s101, 0
	global_load_dword v106, v200, s[100:101] nt
	s_add_u32 s100, s100, 0x6000
	s_addc_u32 s101, s101, 0
	global_load_dword v108, v200, s[100:101] nt
	s_add_u32 s100, s100, 0x6000
	s_addc_u32 s101, s101, 0
	global_load_dword v110, v200, s[100:101] nt
	s_add_u32 s100, s100, 0x6000
	s_addc_u32 s101, s101, 0
	global_load_dword v112, v200, s[100:101] nt
	s_add_u32 s100, s100, 0x6000
	s_addc_u32 s101, s101, 0
	global_load_dword v114, v200, s[100:101] nt
	s_add_u32 s100, s100, 0x6000
	s_addc_u32 s101, s101, 0
	global_load_dword v116, v200, s[100:101] nt
	s_add_u32 s100, s100, 0x6000
	s_addc_u32 s101, s101, 0
	global_load_dword v118, v200, s[100:101] nt
	s_add_u32 s100, s100, 0x6000
	s_addc_u32 s101, s101, 0
	global_load_dword v120, v200, s[100:101] nt
	s_add_u32 s100, s100, 0x6000
	s_addc_u32 s101, s101, 0
	global_load_dword v122, v200, s[100:101] nt
	s_add_u32 s100, s100, 0x6000
	s_addc_u32 s101, s101, 0
	global_load_dword v124, v200, s[100:101] nt
	s_add_u32 s100, s100, 0x6000
	s_addc_u32 s101, s101, 0
	global_load_dword v126, v200, s[100:101] nt
	s_add_u32 s100, s100, 0x6000
	s_addc_u32 s101, s101, 0
	global_load_dword v128, v200, s[100:101] nt
	s_add_u32 s100, s100, 0x6000
	s_addc_u32 s101, s101, 0
	global_load_dword v130, v200, s[100:101] nt
	s_add_u32 s100, s100, 0x6000
	s_addc_u32 s101, s101, 0
	global_load_dword v132, v200, s[100:101] nt
	s_add_u32 s100, s100, 0x6000
	s_addc_u32 s101, s101, 0
	s_mov_b32 s6, 0
.Lada_loop:
	global_load_dword v134, v200, s[100:101] nt
	s_add_u32 s100, s100, 0x6000
	s_addc_u32 s101, s101, 0
	global_load_dword v136, v200, s[100:101] nt
	s_add_u32 s100, s100, 0x6000
	s_addc_u32 s101, s101, 0
	global_load_dword v138, v200, s[100:101] nt
	s_add_u32 s100, s100, 0x6000
	s_addc_u32 s101, s101, 0
	global_load_dword v140, v200, s[100:101] nt
	s_add_u32 s100, s100, 0x6000
	s_addc_u32 s101, s101, 0
	global_load_dword v142, v200, s[100:101] nt
	s_add_u32 s100, s100, 0x6000
	s_addc_u32 s101, s101, 0
	global_load_dword v144, v200, s[100:101] nt
	s_add_u32 s100, s100, 0x6000
	s_addc_u32 s101, s101, 0
	global_load_dword v146, v200, s[100:101] nt
	s_add_u32 s100, s100, 0x6000
	s_addc_u32 s101, s101, 0
	global_load_dword v148, v200, s[100:101] nt
	s_add_u32 s100, s100, 0x6000
	s_addc_u32 s101, s101, 0
	global_load_dword v150, v200, s[100:101] nt
	s_add_u32 s100, s100, 0x6000
	s_addc_u32 s101, s101, 0
	global_load_dword v152, v200, s[100:101] nt
	s_add_u32 s100, s100, 0x6000
	s_addc_u32 s101, s101, 0
	global_load_dword v154, v200, s[100:101] nt
	s_add_u32 s100, s100, 0x6000
	s_addc_u32 s101, s101, 0
	global_load_dword v156, v200, s[100:101] nt
	s_add_u32 s100, s100, 0x6000
	s_addc_u32 s101, s101, 0
	global_load_dword v158, v200, s[100:101] nt
	s_add_u32 s100, s100, 0x6000
	s_addc_u32 s101, s101, 0
	global_load_dword v160, v200, s[100:101] nt
	s_add_u32 s100, s100, 0x6000
	s_addc_u32 s101, s101, 0
	global_load_dword v162, v200, s[100:101] nt
	s_add_u32 s100, s100, 0x6000
	s_addc_u32 s101, s101, 0
	global_load_dword v164, v200, s[100:101] nt
	s_add_u32 s100, s100, 0x6000
	s_addc_u32 s101, s101, 0
	global_load_dword v166, v200, s[100:101] nt
	s_add_u32 s100, s100, 0x6000
	s_addc_u32 s101, s101, 0
	global_load_dword v168, v200, s[100:101] nt
	s_add_u32 s100, s100, 0x6000
	s_addc_u32 s101, s101, 0
	global_load_dword v170, v200, s[100:101] nt
	s_add_u32 s100, s100, 0x6000
	s_addc_u32 s101, s101, 0
	global_load_dword v172, v200, s[100:101] nt
	s_add_u32 s100, s100, 0x6000
	s_addc_u32 s101, s101, 0
	global_load_dword v174, v200, s[100:101] nt
	s_add_u32 s100, s100, 0x6000
	s_addc_u32 s101, s101, 0
	global_load_dword v176, v200, s[100:101] nt
	s_add_u32 s100, s100, 0x6000
	s_addc_u32 s101, s101, 0
	global_load_dword v178, v200, s[100:101] nt
	s_add_u32 s100, s100, 0x6000
	s_addc_u32 s101, s101, 0
	global_load_dword v180, v200, s[100:101] nt
	s_add_u32 s100, s100, 0x6000
	s_addc_u32 s101, s101, 0
	global_load_dword v182, v200, s[100:101] nt
	s_add_u32 s100, s100, 0x6000
	s_addc_u32 s101, s101, 0
	global_load_dword v184, v200, s[100:101] nt
	s_add_u32 s100, s100, 0x6000
	s_addc_u32 s101, s101, 0
	global_load_dword v186, v200, s[100:101] nt
	s_add_u32 s100, s100, 0x6000
	s_addc_u32 s101, s101, 0
	global_load_dword v188, v200, s[100:101] nt
	s_add_u32 s100, s100, 0x6000
	s_addc_u32 s101, s101, 0
	global_load_dword v190, v200, s[100:101] nt
	s_add_u32 s100, s100, 0x6000
	s_addc_u32 s101, s101, 0
	global_load_dword v192, v200, s[100:101] nt
	s_add_u32 s100, s100, 0x6000
	s_addc_u32 s101, s101, 0
	global_load_dword v194, v200, s[100:101] nt
	s_add_u32 s100, s100, 0x6000
	s_addc_u32 s101, s101, 0
	global_load_dword v196, v200, s[100:101] nt
	s_add_u32 s100, s100, 0x6000
	s_addc_u32 s101, s101, 0
	ds_read_b128 v[24:27], v22 offset:4096
	ds_read_b128 v[28:31], v22 offset:8192
	ds_read_b128 v[32:35], v22 offset:12288
	ds_read_b128 v[36:39], v22 offset:16384
	ds_read_b128 v[40:43], v22 offset:20480
	ds_read_b128 v[44:47], v22 offset:24576
	ds_read_b128 v[48:51], v22 offset:28672
	ds_read_b128 v[52:55], v22
	ds_read_b128 v[56:59], v22 offset:32768
	s_waitcnt lgkmcnt(8)
	v_mov_b32_e32 v69, v24
	v_add_u32_e32 v22, 16, v22
	s_waitcnt lgkmcnt(1)
	v_mov_b32_e32 v68, v52
	v_mov_b32_e32 v24, v53
	v_mov_b32_e32 v52, v54
	v_mov_b32_e32 v53, v26
	v_mov_b32_e32 v26, v55
	v_mov_b32_e32 v54, v28
	v_mov_b32_e32 v55, v32
	v_mov_b32_e32 v32, v29
	v_mov_b32_e32 v28, v30
	v_mov_b32_e32 v29, v34
	v_mov_b32_e32 v34, v31
	v_mov_b32_e32 v30, v36
	v_mov_b32_e32 v31, v40
	v_mov_b32_e32 v40, v37
	v_mov_b32_e32 v36, v38
	v_mov_b32_e32 v37, v42
	v_mov_b32_e32 v42, v39
	v_mov_b32_e32 v38, v44
	v_mov_b32_e32 v39, v48
	v_mov_b32_e32 v48, v45
	v_mov_b32_e32 v44, v46
	v_mov_b32_e32 v45, v50
	v_mov_b32_e32 v50, v47
	s_waitcnt vmcnt(60)
	v_pk_fma_f32 v[10:11], v[70:71], v[68:69], v[10:11] op_sel_hi:[0,1,1]
	v_pk_fma_f32 v[12:13], v[70:71], v[54:55], v[12:13] op_sel_hi:[0,1,1]
	v_pk_fma_f32 v[14:15], v[70:71], v[30:31], v[14:15] op_sel_hi:[0,1,1]
	v_pk_fma_f32 v[16:17], v[70:71], v[38:39], v[16:17] op_sel_hi:[0,1,1]
	s_waitcnt lgkmcnt(0)
	v_fmac_f32_e32 v23, v70, v56
	v_pk_fma_f32 v[10:11], v[72:73], v[24:25], v[10:11] op_sel_hi:[0,1,1]
	v_pk_fma_f32 v[12:13], v[72:73], v[32:33], v[12:13] op_sel_hi:[0,1,1]
	v_pk_fma_f32 v[14:15], v[72:73], v[40:41], v[14:15] op_sel_hi:[0,1,1]
	v_pk_fma_f32 v[16:17], v[72:73], v[48:49], v[16:17] op_sel_hi:[0,1,1]
	v_fmac_f32_e32 v23, v72, v57
	v_pk_fma_f32 v[10:11], v[74:75], v[52:53], v[10:11] op_sel_hi:[0,1,1]
	v_pk_fma_f32 v[12:13], v[74:75], v[28:29], v[12:13] op_sel_hi:[0,1,1]
	v_pk_fma_f32 v[14:15], v[74:75], v[36:37], v[14:15] op_sel_hi:[0,1,1]
	v_pk_fma_f32 v[16:17], v[74:75], v[44:45], v[16:17] op_sel_hi:[0,1,1]
	v_fmac_f32_e32 v23, v74, v58
	v_pk_fma_f32 v[10:11], v[76:77], v[26:27], v[10:11] op_sel_hi:[0,1,1]
	v_pk_fma_f32 v[12:13], v[76:77], v[34:35], v[12:13] op_sel_hi:[0,1,1]
	v_pk_fma_f32 v[14:15], v[76:77], v[42:43], v[14:15] op_sel_hi:[0,1,1]
	v_pk_fma_f32 v[16:17], v[76:77], v[50:51], v[16:17] op_sel_hi:[0,1,1]
	v_fmac_f32_e32 v23, v76, v59
	ds_read_b128 v[24:27], v22 offset:4096
	ds_read_b128 v[28:31], v22 offset:8192
	ds_read_b128 v[32:35], v22 offset:12288
	ds_read_b128 v[36:39], v22 offset:16384
	ds_read_b128 v[40:43], v22 offset:20480
	ds_read_b128 v[44:47], v22 offset:24576
	ds_read_b128 v[48:51], v22 offset:28672
	ds_read_b128 v[52:55], v22
	ds_read_b128 v[56:59], v22 offset:32768
	s_waitcnt lgkmcnt(8)
	v_mov_b32_e32 v69, v24
	v_add_u32_e32 v22, 16, v22
	s_waitcnt lgkmcnt(1)
	v_mov_b32_e32 v68, v52
	v_mov_b32_e32 v24, v53
	v_mov_b32_e32 v52, v54
	v_mov_b32_e32 v53, v26
	v_mov_b32_e32 v26, v55
	v_mov_b32_e32 v54, v28
	v_mov_b32_e32 v55, v32
	v_mov_b32_e32 v32, v29
	v_mov_b32_e32 v28, v30
	v_mov_b32_e32 v29, v34
	v_mov_b32_e32 v34, v31
	v_mov_b32_e32 v30, v36
	v_mov_b32_e32 v31, v40
	v_mov_b32_e32 v40, v37
	v_mov_b32_e32 v36, v38
	v_mov_b32_e32 v37, v42
	v_mov_b32_e32 v42, v39
	v_mov_b32_e32 v38, v44
	v_mov_b32_e32 v39, v48
	v_mov_b32_e32 v48, v45
	v_mov_b32_e32 v44, v46
	v_mov_b32_e32 v45, v50
	v_mov_b32_e32 v50, v47
	s_waitcnt vmcnt(56)
	v_pk_fma_f32 v[10:11], v[78:79], v[68:69], v[10:11] op_sel_hi:[0,1,1]
	v_pk_fma_f32 v[12:13], v[78:79], v[54:55], v[12:13] op_sel_hi:[0,1,1]
	v_pk_fma_f32 v[14:15], v[78:79], v[30:31], v[14:15] op_sel_hi:[0,1,1]
	v_pk_fma_f32 v[16:17], v[78:79], v[38:39], v[16:17] op_sel_hi:[0,1,1]
	s_waitcnt lgkmcnt(0)
	v_fmac_f32_e32 v23, v78, v56
	v_pk_fma_f32 v[10:11], v[80:81], v[24:25], v[10:11] op_sel_hi:[0,1,1]
	v_pk_fma_f32 v[12:13], v[80:81], v[32:33], v[12:13] op_sel_hi:[0,1,1]
	v_pk_fma_f32 v[14:15], v[80:81], v[40:41], v[14:15] op_sel_hi:[0,1,1]
	v_pk_fma_f32 v[16:17], v[80:81], v[48:49], v[16:17] op_sel_hi:[0,1,1]
	v_fmac_f32_e32 v23, v80, v57
	v_pk_fma_f32 v[10:11], v[82:83], v[52:53], v[10:11] op_sel_hi:[0,1,1]
	v_pk_fma_f32 v[12:13], v[82:83], v[28:29], v[12:13] op_sel_hi:[0,1,1]
	v_pk_fma_f32 v[14:15], v[82:83], v[36:37], v[14:15] op_sel_hi:[0,1,1]
	v_pk_fma_f32 v[16:17], v[82:83], v[44:45], v[16:17] op_sel_hi:[0,1,1]
	v_fmac_f32_e32 v23, v82, v58
	v_pk_fma_f32 v[10:11], v[84:85], v[26:27], v[10:11] op_sel_hi:[0,1,1]
	v_pk_fma_f32 v[12:13], v[84:85], v[34:35], v[12:13] op_sel_hi:[0,1,1]
	v_pk_fma_f32 v[14:15], v[84:85], v[42:43], v[14:15] op_sel_hi:[0,1,1]
	v_pk_fma_f32 v[16:17], v[84:85], v[50:51], v[16:17] op_sel_hi:[0,1,1]
	v_fmac_f32_e32 v23, v84, v59
	ds_read_b128 v[24:27], v22 offset:4096
	ds_read_b128 v[28:31], v22 offset:8192
	ds_read_b128 v[32:35], v22 offset:12288
	ds_read_b128 v[36:39], v22 offset:16384
	ds_read_b128 v[40:43], v22 offset:20480
	ds_read_b128 v[44:47], v22 offset:24576
	ds_read_b128 v[48:51], v22 offset:28672
	ds_read_b128 v[52:55], v22
	ds_read_b128 v[56:59], v22 offset:32768
	s_waitcnt lgkmcnt(8)
	v_mov_b32_e32 v69, v24
	v_add_u32_e32 v22, 16, v22
	s_waitcnt lgkmcnt(1)
	v_mov_b32_e32 v68, v52
	v_mov_b32_e32 v24, v53
	v_mov_b32_e32 v52, v54
	v_mov_b32_e32 v53, v26
	v_mov_b32_e32 v26, v55
	v_mov_b32_e32 v54, v28
	v_mov_b32_e32 v55, v32
	v_mov_b32_e32 v32, v29
	v_mov_b32_e32 v28, v30
	v_mov_b32_e32 v29, v34
	v_mov_b32_e32 v34, v31
	v_mov_b32_e32 v30, v36
	v_mov_b32_e32 v31, v40
	v_mov_b32_e32 v40, v37
	v_mov_b32_e32 v36, v38
	v_mov_b32_e32 v37, v42
	v_mov_b32_e32 v42, v39
	v_mov_b32_e32 v38, v44
	v_mov_b32_e32 v39, v48
	v_mov_b32_e32 v48, v45
	v_mov_b32_e32 v44, v46
	v_mov_b32_e32 v45, v50
	v_mov_b32_e32 v50, v47
	s_waitcnt vmcnt(52)
	v_pk_fma_f32 v[10:11], v[86:87], v[68:69], v[10:11] op_sel_hi:[0,1,1]
	v_pk_fma_f32 v[12:13], v[86:87], v[54:55], v[12:13] op_sel_hi:[0,1,1]
	v_pk_fma_f32 v[14:15], v[86:87], v[30:31], v[14:15] op_sel_hi:[0,1,1]
	v_pk_fma_f32 v[16:17], v[86:87], v[38:39], v[16:17] op_sel_hi:[0,1,1]
	s_waitcnt lgkmcnt(0)
	v_fmac_f32_e32 v23, v86, v56
	v_pk_fma_f32 v[10:11], v[88:89], v[24:25], v[10:11] op_sel_hi:[0,1,1]
	v_pk_fma_f32 v[12:13], v[88:89], v[32:33], v[12:13] op_sel_hi:[0,1,1]
	v_pk_fma_f32 v[14:15], v[88:89], v[40:41], v[14:15] op_sel_hi:[0,1,1]
	v_pk_fma_f32 v[16:17], v[88:89], v[48:49], v[16:17] op_sel_hi:[0,1,1]
	v_fmac_f32_e32 v23, v88, v57
	v_pk_fma_f32 v[10:11], v[90:91], v[52:53], v[10:11] op_sel_hi:[0,1,1]
	v_pk_fma_f32 v[12:13], v[90:91], v[28:29], v[12:13] op_sel_hi:[0,1,1]
	v_pk_fma_f32 v[14:15], v[90:91], v[36:37], v[14:15] op_sel_hi:[0,1,1]
	v_pk_fma_f32 v[16:17], v[90:91], v[44:45], v[16:17] op_sel_hi:[0,1,1]
	v_fmac_f32_e32 v23, v90, v58
	v_pk_fma_f32 v[10:11], v[92:93], v[26:27], v[10:11] op_sel_hi:[0,1,1]
	v_pk_fma_f32 v[12:13], v[92:93], v[34:35], v[12:13] op_sel_hi:[0,1,1]
	v_pk_fma_f32 v[14:15], v[92:93], v[42:43], v[14:15] op_sel_hi:[0,1,1]
	v_pk_fma_f32 v[16:17], v[92:93], v[50:51], v[16:17] op_sel_hi:[0,1,1]
	v_fmac_f32_e32 v23, v92, v59
	ds_read_b128 v[24:27], v22 offset:4096
	ds_read_b128 v[28:31], v22 offset:8192
	ds_read_b128 v[32:35], v22 offset:12288
	ds_read_b128 v[36:39], v22 offset:16384
	ds_read_b128 v[40:43], v22 offset:20480
	ds_read_b128 v[44:47], v22 offset:24576
	ds_read_b128 v[48:51], v22 offset:28672
	ds_read_b128 v[52:55], v22
	ds_read_b128 v[56:59], v22 offset:32768
	s_waitcnt lgkmcnt(8)
	v_mov_b32_e32 v69, v24
	v_add_u32_e32 v22, 16, v22
	s_waitcnt lgkmcnt(1)
	v_mov_b32_e32 v68, v52
	v_mov_b32_e32 v24, v53
	v_mov_b32_e32 v52, v54
	v_mov_b32_e32 v53, v26
	v_mov_b32_e32 v26, v55
	v_mov_b32_e32 v54, v28
	v_mov_b32_e32 v55, v32
	v_mov_b32_e32 v32, v29
	v_mov_b32_e32 v28, v30
	v_mov_b32_e32 v29, v34
	v_mov_b32_e32 v34, v31
	v_mov_b32_e32 v30, v36
	v_mov_b32_e32 v31, v40
	v_mov_b32_e32 v40, v37
	v_mov_b32_e32 v36, v38
	v_mov_b32_e32 v37, v42
	v_mov_b32_e32 v42, v39
	v_mov_b32_e32 v38, v44
	v_mov_b32_e32 v39, v48
	v_mov_b32_e32 v48, v45
	v_mov_b32_e32 v44, v46
	v_mov_b32_e32 v45, v50
	v_mov_b32_e32 v50, v47
	s_waitcnt vmcnt(48)
	v_pk_fma_f32 v[10:11], v[94:95], v[68:69], v[10:11] op_sel_hi:[0,1,1]
	v_pk_fma_f32 v[12:13], v[94:95], v[54:55], v[12:13] op_sel_hi:[0,1,1]
	v_pk_fma_f32 v[14:15], v[94:95], v[30:31], v[14:15] op_sel_hi:[0,1,1]
	v_pk_fma_f32 v[16:17], v[94:95], v[38:39], v[16:17] op_sel_hi:[0,1,1]
	s_waitcnt lgkmcnt(0)
	v_fmac_f32_e32 v23, v94, v56
	v_pk_fma_f32 v[10:11], v[96:97], v[24:25], v[10:11] op_sel_hi:[0,1,1]
	v_pk_fma_f32 v[12:13], v[96:97], v[32:33], v[12:13] op_sel_hi:[0,1,1]
	v_pk_fma_f32 v[14:15], v[96:97], v[40:41], v[14:15] op_sel_hi:[0,1,1]
	v_pk_fma_f32 v[16:17], v[96:97], v[48:49], v[16:17] op_sel_hi:[0,1,1]
	v_fmac_f32_e32 v23, v96, v57
	v_pk_fma_f32 v[10:11], v[98:99], v[52:53], v[10:11] op_sel_hi:[0,1,1]
	v_pk_fma_f32 v[12:13], v[98:99], v[28:29], v[12:13] op_sel_hi:[0,1,1]
	v_pk_fma_f32 v[14:15], v[98:99], v[36:37], v[14:15] op_sel_hi:[0,1,1]
	v_pk_fma_f32 v[16:17], v[98:99], v[44:45], v[16:17] op_sel_hi:[0,1,1]
	v_fmac_f32_e32 v23, v98, v58
	v_pk_fma_f32 v[10:11], v[100:101], v[26:27], v[10:11] op_sel_hi:[0,1,1]
	v_pk_fma_f32 v[12:13], v[100:101], v[34:35], v[12:13] op_sel_hi:[0,1,1]
	v_pk_fma_f32 v[14:15], v[100:101], v[42:43], v[14:15] op_sel_hi:[0,1,1]
	v_pk_fma_f32 v[16:17], v[100:101], v[50:51], v[16:17] op_sel_hi:[0,1,1]
	v_fmac_f32_e32 v23, v100, v59
	ds_read_b128 v[24:27], v22 offset:4096
	ds_read_b128 v[28:31], v22 offset:8192
	ds_read_b128 v[32:35], v22 offset:12288
	ds_read_b128 v[36:39], v22 offset:16384
	ds_read_b128 v[40:43], v22 offset:20480
	ds_read_b128 v[44:47], v22 offset:24576
	ds_read_b128 v[48:51], v22 offset:28672
	ds_read_b128 v[52:55], v22
	ds_read_b128 v[56:59], v22 offset:32768
	s_waitcnt lgkmcnt(8)
	v_mov_b32_e32 v69, v24
	v_add_u32_e32 v22, 16, v22
	s_waitcnt lgkmcnt(1)
	v_mov_b32_e32 v68, v52
	v_mov_b32_e32 v24, v53
	v_mov_b32_e32 v52, v54
	v_mov_b32_e32 v53, v26
	v_mov_b32_e32 v26, v55
	v_mov_b32_e32 v54, v28
	v_mov_b32_e32 v55, v32
	v_mov_b32_e32 v32, v29
	v_mov_b32_e32 v28, v30
	v_mov_b32_e32 v29, v34
	v_mov_b32_e32 v34, v31
	v_mov_b32_e32 v30, v36
	v_mov_b32_e32 v31, v40
	v_mov_b32_e32 v40, v37
	v_mov_b32_e32 v36, v38
	v_mov_b32_e32 v37, v42
	v_mov_b32_e32 v42, v39
	v_mov_b32_e32 v38, v44
	v_mov_b32_e32 v39, v48
	v_mov_b32_e32 v48, v45
	v_mov_b32_e32 v44, v46
	v_mov_b32_e32 v45, v50
	v_mov_b32_e32 v50, v47
	s_waitcnt vmcnt(44)
	v_pk_fma_f32 v[10:11], v[102:103], v[68:69], v[10:11] op_sel_hi:[0,1,1]
	v_pk_fma_f32 v[12:13], v[102:103], v[54:55], v[12:13] op_sel_hi:[0,1,1]
	v_pk_fma_f32 v[14:15], v[102:103], v[30:31], v[14:15] op_sel_hi:[0,1,1]
	v_pk_fma_f32 v[16:17], v[102:103], v[38:39], v[16:17] op_sel_hi:[0,1,1]
	s_waitcnt lgkmcnt(0)
	v_fmac_f32_e32 v23, v102, v56
	v_pk_fma_f32 v[10:11], v[104:105], v[24:25], v[10:11] op_sel_hi:[0,1,1]
	v_pk_fma_f32 v[12:13], v[104:105], v[32:33], v[12:13] op_sel_hi:[0,1,1]
	v_pk_fma_f32 v[14:15], v[104:105], v[40:41], v[14:15] op_sel_hi:[0,1,1]
	v_pk_fma_f32 v[16:17], v[104:105], v[48:49], v[16:17] op_sel_hi:[0,1,1]
	v_fmac_f32_e32 v23, v104, v57
	v_pk_fma_f32 v[10:11], v[106:107], v[52:53], v[10:11] op_sel_hi:[0,1,1]
	v_pk_fma_f32 v[12:13], v[106:107], v[28:29], v[12:13] op_sel_hi:[0,1,1]
	v_pk_fma_f32 v[14:15], v[106:107], v[36:37], v[14:15] op_sel_hi:[0,1,1]
	v_pk_fma_f32 v[16:17], v[106:107], v[44:45], v[16:17] op_sel_hi:[0,1,1]
	v_fmac_f32_e32 v23, v106, v58
	v_pk_fma_f32 v[10:11], v[108:109], v[26:27], v[10:11] op_sel_hi:[0,1,1]
	v_pk_fma_f32 v[12:13], v[108:109], v[34:35], v[12:13] op_sel_hi:[0,1,1]
	v_pk_fma_f32 v[14:15], v[108:109], v[42:43], v[14:15] op_sel_hi:[0,1,1]
	v_pk_fma_f32 v[16:17], v[108:109], v[50:51], v[16:17] op_sel_hi:[0,1,1]
	v_fmac_f32_e32 v23, v108, v59
	ds_read_b128 v[24:27], v22 offset:4096
	ds_read_b128 v[28:31], v22 offset:8192
	ds_read_b128 v[32:35], v22 offset:12288
	ds_read_b128 v[36:39], v22 offset:16384
	ds_read_b128 v[40:43], v22 offset:20480
	ds_read_b128 v[44:47], v22 offset:24576
	ds_read_b128 v[48:51], v22 offset:28672
	ds_read_b128 v[52:55], v22
	ds_read_b128 v[56:59], v22 offset:32768
	s_waitcnt lgkmcnt(8)
	v_mov_b32_e32 v69, v24
	v_add_u32_e32 v22, 16, v22
	s_waitcnt lgkmcnt(1)
	v_mov_b32_e32 v68, v52
	v_mov_b32_e32 v24, v53
	v_mov_b32_e32 v52, v54
	v_mov_b32_e32 v53, v26
	v_mov_b32_e32 v26, v55
	v_mov_b32_e32 v54, v28
	v_mov_b32_e32 v55, v32
	v_mov_b32_e32 v32, v29
	v_mov_b32_e32 v28, v30
	v_mov_b32_e32 v29, v34
	v_mov_b32_e32 v34, v31
	v_mov_b32_e32 v30, v36
	v_mov_b32_e32 v31, v40
	v_mov_b32_e32 v40, v37
	v_mov_b32_e32 v36, v38
	v_mov_b32_e32 v37, v42
	v_mov_b32_e32 v42, v39
	v_mov_b32_e32 v38, v44
	v_mov_b32_e32 v39, v48
	v_mov_b32_e32 v48, v45
	v_mov_b32_e32 v44, v46
	v_mov_b32_e32 v45, v50
	v_mov_b32_e32 v50, v47
	s_waitcnt vmcnt(40)
	v_pk_fma_f32 v[10:11], v[110:111], v[68:69], v[10:11] op_sel_hi:[0,1,1]
	v_pk_fma_f32 v[12:13], v[110:111], v[54:55], v[12:13] op_sel_hi:[0,1,1]
	v_pk_fma_f32 v[14:15], v[110:111], v[30:31], v[14:15] op_sel_hi:[0,1,1]
	v_pk_fma_f32 v[16:17], v[110:111], v[38:39], v[16:17] op_sel_hi:[0,1,1]
	s_waitcnt lgkmcnt(0)
	v_fmac_f32_e32 v23, v110, v56
	v_pk_fma_f32 v[10:11], v[112:113], v[24:25], v[10:11] op_sel_hi:[0,1,1]
	v_pk_fma_f32 v[12:13], v[112:113], v[32:33], v[12:13] op_sel_hi:[0,1,1]
	v_pk_fma_f32 v[14:15], v[112:113], v[40:41], v[14:15] op_sel_hi:[0,1,1]
	v_pk_fma_f32 v[16:17], v[112:113], v[48:49], v[16:17] op_sel_hi:[0,1,1]
	v_fmac_f32_e32 v23, v112, v57
	v_pk_fma_f32 v[10:11], v[114:115], v[52:53], v[10:11] op_sel_hi:[0,1,1]
	v_pk_fma_f32 v[12:13], v[114:115], v[28:29], v[12:13] op_sel_hi:[0,1,1]
	v_pk_fma_f32 v[14:15], v[114:115], v[36:37], v[14:15] op_sel_hi:[0,1,1]
	v_pk_fma_f32 v[16:17], v[114:115], v[44:45], v[16:17] op_sel_hi:[0,1,1]
	v_fmac_f32_e32 v23, v114, v58
	v_pk_fma_f32 v[10:11], v[116:117], v[26:27], v[10:11] op_sel_hi:[0,1,1]
	v_pk_fma_f32 v[12:13], v[116:117], v[34:35], v[12:13] op_sel_hi:[0,1,1]
	v_pk_fma_f32 v[14:15], v[116:117], v[42:43], v[14:15] op_sel_hi:[0,1,1]
	v_pk_fma_f32 v[16:17], v[116:117], v[50:51], v[16:17] op_sel_hi:[0,1,1]
	v_fmac_f32_e32 v23, v116, v59
	ds_read_b128 v[24:27], v22 offset:4096
	ds_read_b128 v[28:31], v22 offset:8192
	ds_read_b128 v[32:35], v22 offset:12288
	ds_read_b128 v[36:39], v22 offset:16384
	ds_read_b128 v[40:43], v22 offset:20480
	ds_read_b128 v[44:47], v22 offset:24576
	ds_read_b128 v[48:51], v22 offset:28672
	ds_read_b128 v[52:55], v22
	ds_read_b128 v[56:59], v22 offset:32768
	s_waitcnt lgkmcnt(8)
	v_mov_b32_e32 v69, v24
	v_add_u32_e32 v22, 16, v22
	s_waitcnt lgkmcnt(1)
	v_mov_b32_e32 v68, v52
	v_mov_b32_e32 v24, v53
	v_mov_b32_e32 v52, v54
	v_mov_b32_e32 v53, v26
	v_mov_b32_e32 v26, v55
	v_mov_b32_e32 v54, v28
	v_mov_b32_e32 v55, v32
	v_mov_b32_e32 v32, v29
	v_mov_b32_e32 v28, v30
	v_mov_b32_e32 v29, v34
	v_mov_b32_e32 v34, v31
	v_mov_b32_e32 v30, v36
	v_mov_b32_e32 v31, v40
	v_mov_b32_e32 v40, v37
	v_mov_b32_e32 v36, v38
	v_mov_b32_e32 v37, v42
	v_mov_b32_e32 v42, v39
	v_mov_b32_e32 v38, v44
	v_mov_b32_e32 v39, v48
	v_mov_b32_e32 v48, v45
	v_mov_b32_e32 v44, v46
	v_mov_b32_e32 v45, v50
	v_mov_b32_e32 v50, v47
	s_waitcnt vmcnt(36)
	v_pk_fma_f32 v[10:11], v[118:119], v[68:69], v[10:11] op_sel_hi:[0,1,1]
	v_pk_fma_f32 v[12:13], v[118:119], v[54:55], v[12:13] op_sel_hi:[0,1,1]
	v_pk_fma_f32 v[14:15], v[118:119], v[30:31], v[14:15] op_sel_hi:[0,1,1]
	v_pk_fma_f32 v[16:17], v[118:119], v[38:39], v[16:17] op_sel_hi:[0,1,1]
	s_waitcnt lgkmcnt(0)
	v_fmac_f32_e32 v23, v118, v56
	v_pk_fma_f32 v[10:11], v[120:121], v[24:25], v[10:11] op_sel_hi:[0,1,1]
	v_pk_fma_f32 v[12:13], v[120:121], v[32:33], v[12:13] op_sel_hi:[0,1,1]
	v_pk_fma_f32 v[14:15], v[120:121], v[40:41], v[14:15] op_sel_hi:[0,1,1]
	v_pk_fma_f32 v[16:17], v[120:121], v[48:49], v[16:17] op_sel_hi:[0,1,1]
	v_fmac_f32_e32 v23, v120, v57
	v_pk_fma_f32 v[10:11], v[122:123], v[52:53], v[10:11] op_sel_hi:[0,1,1]
	v_pk_fma_f32 v[12:13], v[122:123], v[28:29], v[12:13] op_sel_hi:[0,1,1]
	v_pk_fma_f32 v[14:15], v[122:123], v[36:37], v[14:15] op_sel_hi:[0,1,1]
	v_pk_fma_f32 v[16:17], v[122:123], v[44:45], v[16:17] op_sel_hi:[0,1,1]
	v_fmac_f32_e32 v23, v122, v58
	v_pk_fma_f32 v[10:11], v[124:125], v[26:27], v[10:11] op_sel_hi:[0,1,1]
	v_pk_fma_f32 v[12:13], v[124:125], v[34:35], v[12:13] op_sel_hi:[0,1,1]
	v_pk_fma_f32 v[14:15], v[124:125], v[42:43], v[14:15] op_sel_hi:[0,1,1]
	v_pk_fma_f32 v[16:17], v[124:125], v[50:51], v[16:17] op_sel_hi:[0,1,1]
	v_fmac_f32_e32 v23, v124, v59
	ds_read_b128 v[24:27], v22 offset:4096
	ds_read_b128 v[28:31], v22 offset:8192
	ds_read_b128 v[32:35], v22 offset:12288
	ds_read_b128 v[36:39], v22 offset:16384
	ds_read_b128 v[40:43], v22 offset:20480
	ds_read_b128 v[44:47], v22 offset:24576
	ds_read_b128 v[48:51], v22 offset:28672
	ds_read_b128 v[52:55], v22
	ds_read_b128 v[56:59], v22 offset:32768
	s_waitcnt lgkmcnt(8)
	v_mov_b32_e32 v69, v24
	v_add_u32_e32 v22, 16, v22
	s_waitcnt lgkmcnt(1)
	v_mov_b32_e32 v68, v52
	v_mov_b32_e32 v24, v53
	v_mov_b32_e32 v52, v54
	v_mov_b32_e32 v53, v26
	v_mov_b32_e32 v26, v55
	v_mov_b32_e32 v54, v28
	v_mov_b32_e32 v55, v32
	v_mov_b32_e32 v32, v29
	v_mov_b32_e32 v28, v30
	v_mov_b32_e32 v29, v34
	v_mov_b32_e32 v34, v31
	v_mov_b32_e32 v30, v36
	v_mov_b32_e32 v31, v40
	v_mov_b32_e32 v40, v37
	v_mov_b32_e32 v36, v38
	v_mov_b32_e32 v37, v42
	v_mov_b32_e32 v42, v39
	v_mov_b32_e32 v38, v44
	v_mov_b32_e32 v39, v48
	v_mov_b32_e32 v48, v45
	v_mov_b32_e32 v44, v46
	v_mov_b32_e32 v45, v50
	v_mov_b32_e32 v50, v47
	s_waitcnt vmcnt(32)
	v_pk_fma_f32 v[10:11], v[126:127], v[68:69], v[10:11] op_sel_hi:[0,1,1]
	v_pk_fma_f32 v[12:13], v[126:127], v[54:55], v[12:13] op_sel_hi:[0,1,1]
	v_pk_fma_f32 v[14:15], v[126:127], v[30:31], v[14:15] op_sel_hi:[0,1,1]
	v_pk_fma_f32 v[16:17], v[126:127], v[38:39], v[16:17] op_sel_hi:[0,1,1]
	s_waitcnt lgkmcnt(0)
	v_fmac_f32_e32 v23, v126, v56
	v_pk_fma_f32 v[10:11], v[128:129], v[24:25], v[10:11] op_sel_hi:[0,1,1]
	v_pk_fma_f32 v[12:13], v[128:129], v[32:33], v[12:13] op_sel_hi:[0,1,1]
	v_pk_fma_f32 v[14:15], v[128:129], v[40:41], v[14:15] op_sel_hi:[0,1,1]
	v_pk_fma_f32 v[16:17], v[128:129], v[48:49], v[16:17] op_sel_hi:[0,1,1]
	v_fmac_f32_e32 v23, v128, v57
	v_pk_fma_f32 v[10:11], v[130:131], v[52:53], v[10:11] op_sel_hi:[0,1,1]
	v_pk_fma_f32 v[12:13], v[130:131], v[28:29], v[12:13] op_sel_hi:[0,1,1]
	v_pk_fma_f32 v[14:15], v[130:131], v[36:37], v[14:15] op_sel_hi:[0,1,1]
	v_pk_fma_f32 v[16:17], v[130:131], v[44:45], v[16:17] op_sel_hi:[0,1,1]
	v_fmac_f32_e32 v23, v130, v58
	v_pk_fma_f32 v[10:11], v[132:133], v[26:27], v[10:11] op_sel_hi:[0,1,1]
	v_pk_fma_f32 v[12:13], v[132:133], v[34:35], v[12:13] op_sel_hi:[0,1,1]
	v_pk_fma_f32 v[14:15], v[132:133], v[42:43], v[14:15] op_sel_hi:[0,1,1]
	v_pk_fma_f32 v[16:17], v[132:133], v[50:51], v[16:17] op_sel_hi:[0,1,1]
	v_fmac_f32_e32 v23, v132, v59
	s_cmp_eq_u32 s6, 3
	s_cbranch_scc0 .Lada_more
	v_readfirstlane_b32 s100, v8
	v_readfirstlane_b32 s101, v9
	s_nop 4
.Lada_more:
	global_load_dword v70, v200, s[100:101] nt
	s_add_u32 s100, s100, 0x6000
	s_addc_u32 s101, s101, 0
	global_load_dword v72, v200, s[100:101] nt
	s_add_u32 s100, s100, 0x6000
	s_addc_u32 s101, s101, 0
	global_load_dword v74, v200, s[100:101] nt
	s_add_u32 s100, s100, 0x6000
	s_addc_u32 s101, s101, 0
	global_load_dword v76, v200, s[100:101] nt
	s_add_u32 s100, s100, 0x6000
	s_addc_u32 s101, s101, 0
	global_load_dword v78, v200, s[100:101] nt
	s_add_u32 s100, s100, 0x6000
	s_addc_u32 s101, s101, 0
	global_load_dword v80, v200, s[100:101] nt
	s_add_u32 s100, s100, 0x6000
	s_addc_u32 s101, s101, 0
	global_load_dword v82, v200, s[100:101] nt
	s_add_u32 s100, s100, 0x6000
	s_addc_u32 s101, s101, 0
	global_load_dword v84, v200, s[100:101] nt
	s_add_u32 s100, s100, 0x6000
	s_addc_u32 s101, s101, 0
	global_load_dword v86, v200, s[100:101] nt
	s_add_u32 s100, s100, 0x6000
	s_addc_u32 s101, s101, 0
	global_load_dword v88, v200, s[100:101] nt
	s_add_u32 s100, s100, 0x6000
	s_addc_u32 s101, s101, 0
	global_load_dword v90, v200, s[100:101] nt
	s_add_u32 s100, s100, 0x6000
	s_addc_u32 s101, s101, 0
	global_load_dword v92, v200, s[100:101] nt
	s_add_u32 s100, s100, 0x6000
	s_addc_u32 s101, s101, 0
	global_load_dword v94, v200, s[100:101] nt
	s_add_u32 s100, s100, 0x6000
	s_addc_u32 s101, s101, 0
	global_load_dword v96, v200, s[100:101] nt
	s_add_u32 s100, s100, 0x6000
	s_addc_u32 s101, s101, 0
	global_load_dword v98, v200, s[100:101] nt
	s_add_u32 s100, s100, 0x6000
	s_addc_u32 s101, s101, 0
	global_load_dword v100, v200, s[100:101] nt
	s_add_u32 s100, s100, 0x6000
	s_addc_u32 s101, s101, 0
	global_load_dword v102, v200, s[100:101] nt
	s_add_u32 s100, s100, 0x6000
	s_addc_u32 s101, s101, 0
	global_load_dword v104, v200, s[100:101] nt
	s_add_u32 s100, s100, 0x6000
	s_addc_u32 s101, s101, 0
	global_load_dword v106, v200, s[100:101] nt
	s_add_u32 s100, s100, 0x6000
	s_addc_u32 s101, s101, 0
	global_load_dword v108, v200, s[100:101] nt
	s_add_u32 s100, s100, 0x6000
	s_addc_u32 s101, s101, 0
	global_load_dword v110, v200, s[100:101] nt
	s_add_u32 s100, s100, 0x6000
	s_addc_u32 s101, s101, 0
	global_load_dword v112, v200, s[100:101] nt
	s_add_u32 s100, s100, 0x6000
	s_addc_u32 s101, s101, 0
	global_load_dword v114, v200, s[100:101] nt
	s_add_u32 s100, s100, 0x6000
	s_addc_u32 s101, s101, 0
	global_load_dword v116, v200, s[100:101] nt
	s_add_u32 s100, s100, 0x6000
	s_addc_u32 s101, s101, 0
	global_load_dword v118, v200, s[100:101] nt
	s_add_u32 s100, s100, 0x6000
	s_addc_u32 s101, s101, 0
	global_load_dword v120, v200, s[100:101] nt
	s_add_u32 s100, s100, 0x6000
	s_addc_u32 s101, s101, 0
	global_load_dword v122, v200, s[100:101] nt
	s_add_u32 s100, s100, 0x6000
	s_addc_u32 s101, s101, 0
	global_load_dword v124, v200, s[100:101] nt
	s_add_u32 s100, s100, 0x6000
	s_addc_u32 s101, s101, 0
	global_load_dword v126, v200, s[100:101] nt
	s_add_u32 s100, s100, 0x6000
	s_addc_u32 s101, s101, 0
	global_load_dword v128, v200, s[100:101] nt
	s_add_u32 s100, s100, 0x6000
	s_addc_u32 s101, s101, 0
	global_load_dword v130, v200, s[100:101] nt
	s_add_u32 s100, s100, 0x6000
	s_addc_u32 s101, s101, 0
	global_load_dword v132, v200, s[100:101] nt
	s_add_u32 s100, s100, 0x6000
	s_addc_u32 s101, s101, 0
	ds_read_b128 v[24:27], v22 offset:4096
	ds_read_b128 v[28:31], v22 offset:8192
	ds_read_b128 v[32:35], v22 offset:12288
	ds_read_b128 v[36:39], v22 offset:16384
	ds_read_b128 v[40:43], v22 offset:20480
	ds_read_b128 v[44:47], v22 offset:24576
	ds_read_b128 v[48:51], v22 offset:28672
	ds_read_b128 v[52:55], v22
	ds_read_b128 v[56:59], v22 offset:32768
	s_waitcnt lgkmcnt(8)
	v_mov_b32_e32 v69, v24
	v_add_u32_e32 v22, 16, v22
	s_waitcnt lgkmcnt(1)
	v_mov_b32_e32 v68, v52
	v_mov_b32_e32 v24, v53
	v_mov_b32_e32 v52, v54
	v_mov_b32_e32 v53, v26
	v_mov_b32_e32 v26, v55
	v_mov_b32_e32 v54, v28
	v_mov_b32_e32 v55, v32
	v_mov_b32_e32 v32, v29
	v_mov_b32_e32 v28, v30
	v_mov_b32_e32 v29, v34
	v_mov_b32_e32 v34, v31
	v_mov_b32_e32 v30, v36
	v_mov_b32_e32 v31, v40
	v_mov_b32_e32 v40, v37
	v_mov_b32_e32 v36, v38
	v_mov_b32_e32 v37, v42
	v_mov_b32_e32 v42, v39
	v_mov_b32_e32 v38, v44
	v_mov_b32_e32 v39, v48
	v_mov_b32_e32 v48, v45
	v_mov_b32_e32 v44, v46
	v_mov_b32_e32 v45, v50
	v_mov_b32_e32 v50, v47
	s_waitcnt vmcnt(60)
	v_pk_fma_f32 v[10:11], v[134:135], v[68:69], v[10:11] op_sel_hi:[0,1,1]
	v_pk_fma_f32 v[12:13], v[134:135], v[54:55], v[12:13] op_sel_hi:[0,1,1]
	v_pk_fma_f32 v[14:15], v[134:135], v[30:31], v[14:15] op_sel_hi:[0,1,1]
	v_pk_fma_f32 v[16:17], v[134:135], v[38:39], v[16:17] op_sel_hi:[0,1,1]
	s_waitcnt lgkmcnt(0)
	v_fmac_f32_e32 v23, v134, v56
	v_pk_fma_f32 v[10:11], v[136:137], v[24:25], v[10:11] op_sel_hi:[0,1,1]
	v_pk_fma_f32 v[12:13], v[136:137], v[32:33], v[12:13] op_sel_hi:[0,1,1]
	v_pk_fma_f32 v[14:15], v[136:137], v[40:41], v[14:15] op_sel_hi:[0,1,1]
	v_pk_fma_f32 v[16:17], v[136:137], v[48:49], v[16:17] op_sel_hi:[0,1,1]
	v_fmac_f32_e32 v23, v136, v57
	v_pk_fma_f32 v[10:11], v[138:139], v[52:53], v[10:11] op_sel_hi:[0,1,1]
	v_pk_fma_f32 v[12:13], v[138:139], v[28:29], v[12:13] op_sel_hi:[0,1,1]
	v_pk_fma_f32 v[14:15], v[138:139], v[36:37], v[14:15] op_sel_hi:[0,1,1]
	v_pk_fma_f32 v[16:17], v[138:139], v[44:45], v[16:17] op_sel_hi:[0,1,1]
	v_fmac_f32_e32 v23, v138, v58
	v_pk_fma_f32 v[10:11], v[140:141], v[26:27], v[10:11] op_sel_hi:[0,1,1]
	v_pk_fma_f32 v[12:13], v[140:141], v[34:35], v[12:13] op_sel_hi:[0,1,1]
	v_pk_fma_f32 v[14:15], v[140:141], v[42:43], v[14:15] op_sel_hi:[0,1,1]
	v_pk_fma_f32 v[16:17], v[140:141], v[50:51], v[16:17] op_sel_hi:[0,1,1]
	v_fmac_f32_e32 v23, v140, v59
	ds_read_b128 v[24:27], v22 offset:4096
	ds_read_b128 v[28:31], v22 offset:8192
	ds_read_b128 v[32:35], v22 offset:12288
	ds_read_b128 v[36:39], v22 offset:16384
	ds_read_b128 v[40:43], v22 offset:20480
	ds_read_b128 v[44:47], v22 offset:24576
	ds_read_b128 v[48:51], v22 offset:28672
	ds_read_b128 v[52:55], v22
	ds_read_b128 v[56:59], v22 offset:32768
	s_waitcnt lgkmcnt(8)
	v_mov_b32_e32 v69, v24
	v_add_u32_e32 v22, 16, v22
	s_waitcnt lgkmcnt(1)
	v_mov_b32_e32 v68, v52
	v_mov_b32_e32 v24, v53
	v_mov_b32_e32 v52, v54
	v_mov_b32_e32 v53, v26
	v_mov_b32_e32 v26, v55
	v_mov_b32_e32 v54, v28
	v_mov_b32_e32 v55, v32
	v_mov_b32_e32 v32, v29
	v_mov_b32_e32 v28, v30
	v_mov_b32_e32 v29, v34
	v_mov_b32_e32 v34, v31
	v_mov_b32_e32 v30, v36
	v_mov_b32_e32 v31, v40
	v_mov_b32_e32 v40, v37
	v_mov_b32_e32 v36, v38
	v_mov_b32_e32 v37, v42
	v_mov_b32_e32 v42, v39
	v_mov_b32_e32 v38, v44
	v_mov_b32_e32 v39, v48
	v_mov_b32_e32 v48, v45
	v_mov_b32_e32 v44, v46
	v_mov_b32_e32 v45, v50
	v_mov_b32_e32 v50, v47
	s_waitcnt vmcnt(56)
	v_pk_fma_f32 v[10:11], v[142:143], v[68:69], v[10:11] op_sel_hi:[0,1,1]
	v_pk_fma_f32 v[12:13], v[142:143], v[54:55], v[12:13] op_sel_hi:[0,1,1]
	v_pk_fma_f32 v[14:15], v[142:143], v[30:31], v[14:15] op_sel_hi:[0,1,1]
	v_pk_fma_f32 v[16:17], v[142:143], v[38:39], v[16:17] op_sel_hi:[0,1,1]
	s_waitcnt lgkmcnt(0)
	v_fmac_f32_e32 v23, v142, v56
	v_pk_fma_f32 v[10:11], v[144:145], v[24:25], v[10:11] op_sel_hi:[0,1,1]
	v_pk_fma_f32 v[12:13], v[144:145], v[32:33], v[12:13] op_sel_hi:[0,1,1]
	v_pk_fma_f32 v[14:15], v[144:145], v[40:41], v[14:15] op_sel_hi:[0,1,1]
	v_pk_fma_f32 v[16:17], v[144:145], v[48:49], v[16:17] op_sel_hi:[0,1,1]
	v_fmac_f32_e32 v23, v144, v57
	v_pk_fma_f32 v[10:11], v[146:147], v[52:53], v[10:11] op_sel_hi:[0,1,1]
	v_pk_fma_f32 v[12:13], v[146:147], v[28:29], v[12:13] op_sel_hi:[0,1,1]
	v_pk_fma_f32 v[14:15], v[146:147], v[36:37], v[14:15] op_sel_hi:[0,1,1]
	v_pk_fma_f32 v[16:17], v[146:147], v[44:45], v[16:17] op_sel_hi:[0,1,1]
	v_fmac_f32_e32 v23, v146, v58
	v_pk_fma_f32 v[10:11], v[148:149], v[26:27], v[10:11] op_sel_hi:[0,1,1]
	v_pk_fma_f32 v[12:13], v[148:149], v[34:35], v[12:13] op_sel_hi:[0,1,1]
	v_pk_fma_f32 v[14:15], v[148:149], v[42:43], v[14:15] op_sel_hi:[0,1,1]
	v_pk_fma_f32 v[16:17], v[148:149], v[50:51], v[16:17] op_sel_hi:[0,1,1]
	v_fmac_f32_e32 v23, v148, v59
	ds_read_b128 v[24:27], v22 offset:4096
	ds_read_b128 v[28:31], v22 offset:8192
	ds_read_b128 v[32:35], v22 offset:12288
	ds_read_b128 v[36:39], v22 offset:16384
	ds_read_b128 v[40:43], v22 offset:20480
	ds_read_b128 v[44:47], v22 offset:24576
	ds_read_b128 v[48:51], v22 offset:28672
	ds_read_b128 v[52:55], v22
	ds_read_b128 v[56:59], v22 offset:32768
	s_waitcnt lgkmcnt(8)
	v_mov_b32_e32 v69, v24
	v_add_u32_e32 v22, 16, v22
	s_waitcnt lgkmcnt(1)
	v_mov_b32_e32 v68, v52
	v_mov_b32_e32 v24, v53
	v_mov_b32_e32 v52, v54
	v_mov_b32_e32 v53, v26
	v_mov_b32_e32 v26, v55
	v_mov_b32_e32 v54, v28
	v_mov_b32_e32 v55, v32
	v_mov_b32_e32 v32, v29
	v_mov_b32_e32 v28, v30
	v_mov_b32_e32 v29, v34
	v_mov_b32_e32 v34, v31
	v_mov_b32_e32 v30, v36
	v_mov_b32_e32 v31, v40
	v_mov_b32_e32 v40, v37
	v_mov_b32_e32 v36, v38
	v_mov_b32_e32 v37, v42
	v_mov_b32_e32 v42, v39
	v_mov_b32_e32 v38, v44
	v_mov_b32_e32 v39, v48
	v_mov_b32_e32 v48, v45
	v_mov_b32_e32 v44, v46
	v_mov_b32_e32 v45, v50
	v_mov_b32_e32 v50, v47
	s_waitcnt vmcnt(52)
	v_pk_fma_f32 v[10:11], v[150:151], v[68:69], v[10:11] op_sel_hi:[0,1,1]
	v_pk_fma_f32 v[12:13], v[150:151], v[54:55], v[12:13] op_sel_hi:[0,1,1]
	v_pk_fma_f32 v[14:15], v[150:151], v[30:31], v[14:15] op_sel_hi:[0,1,1]
	v_pk_fma_f32 v[16:17], v[150:151], v[38:39], v[16:17] op_sel_hi:[0,1,1]
	s_waitcnt lgkmcnt(0)
	v_fmac_f32_e32 v23, v150, v56
	v_pk_fma_f32 v[10:11], v[152:153], v[24:25], v[10:11] op_sel_hi:[0,1,1]
	v_pk_fma_f32 v[12:13], v[152:153], v[32:33], v[12:13] op_sel_hi:[0,1,1]
	v_pk_fma_f32 v[14:15], v[152:153], v[40:41], v[14:15] op_sel_hi:[0,1,1]
	v_pk_fma_f32 v[16:17], v[152:153], v[48:49], v[16:17] op_sel_hi:[0,1,1]
	v_fmac_f32_e32 v23, v152, v57
	v_pk_fma_f32 v[10:11], v[154:155], v[52:53], v[10:11] op_sel_hi:[0,1,1]
	v_pk_fma_f32 v[12:13], v[154:155], v[28:29], v[12:13] op_sel_hi:[0,1,1]
	v_pk_fma_f32 v[14:15], v[154:155], v[36:37], v[14:15] op_sel_hi:[0,1,1]
	v_pk_fma_f32 v[16:17], v[154:155], v[44:45], v[16:17] op_sel_hi:[0,1,1]
	v_fmac_f32_e32 v23, v154, v58
	v_pk_fma_f32 v[10:11], v[156:157], v[26:27], v[10:11] op_sel_hi:[0,1,1]
	v_pk_fma_f32 v[12:13], v[156:157], v[34:35], v[12:13] op_sel_hi:[0,1,1]
	v_pk_fma_f32 v[14:15], v[156:157], v[42:43], v[14:15] op_sel_hi:[0,1,1]
	v_pk_fma_f32 v[16:17], v[156:157], v[50:51], v[16:17] op_sel_hi:[0,1,1]
	v_fmac_f32_e32 v23, v156, v59
	ds_read_b128 v[24:27], v22 offset:4096
	ds_read_b128 v[28:31], v22 offset:8192
	ds_read_b128 v[32:35], v22 offset:12288
	ds_read_b128 v[36:39], v22 offset:16384
	ds_read_b128 v[40:43], v22 offset:20480
	ds_read_b128 v[44:47], v22 offset:24576
	ds_read_b128 v[48:51], v22 offset:28672
	ds_read_b128 v[52:55], v22
	ds_read_b128 v[56:59], v22 offset:32768
	s_waitcnt lgkmcnt(8)
	v_mov_b32_e32 v69, v24
	v_add_u32_e32 v22, 16, v22
	s_waitcnt lgkmcnt(1)
	v_mov_b32_e32 v68, v52
	v_mov_b32_e32 v24, v53
	v_mov_b32_e32 v52, v54
	v_mov_b32_e32 v53, v26
	v_mov_b32_e32 v26, v55
	v_mov_b32_e32 v54, v28
	v_mov_b32_e32 v55, v32
	v_mov_b32_e32 v32, v29
	v_mov_b32_e32 v28, v30
	v_mov_b32_e32 v29, v34
	v_mov_b32_e32 v34, v31
	v_mov_b32_e32 v30, v36
	v_mov_b32_e32 v31, v40
	v_mov_b32_e32 v40, v37
	v_mov_b32_e32 v36, v38
	v_mov_b32_e32 v37, v42
	v_mov_b32_e32 v42, v39
	v_mov_b32_e32 v38, v44
	v_mov_b32_e32 v39, v48
	v_mov_b32_e32 v48, v45
	v_mov_b32_e32 v44, v46
	v_mov_b32_e32 v45, v50
	v_mov_b32_e32 v50, v47
	s_waitcnt vmcnt(48)
	v_pk_fma_f32 v[10:11], v[158:159], v[68:69], v[10:11] op_sel_hi:[0,1,1]
	v_pk_fma_f32 v[12:13], v[158:159], v[54:55], v[12:13] op_sel_hi:[0,1,1]
	v_pk_fma_f32 v[14:15], v[158:159], v[30:31], v[14:15] op_sel_hi:[0,1,1]
	v_pk_fma_f32 v[16:17], v[158:159], v[38:39], v[16:17] op_sel_hi:[0,1,1]
	s_waitcnt lgkmcnt(0)
	v_fmac_f32_e32 v23, v158, v56
	v_pk_fma_f32 v[10:11], v[160:161], v[24:25], v[10:11] op_sel_hi:[0,1,1]
	v_pk_fma_f32 v[12:13], v[160:161], v[32:33], v[12:13] op_sel_hi:[0,1,1]
	v_pk_fma_f32 v[14:15], v[160:161], v[40:41], v[14:15] op_sel_hi:[0,1,1]
	v_pk_fma_f32 v[16:17], v[160:161], v[48:49], v[16:17] op_sel_hi:[0,1,1]
	v_fmac_f32_e32 v23, v160, v57
	v_pk_fma_f32 v[10:11], v[162:163], v[52:53], v[10:11] op_sel_hi:[0,1,1]
	v_pk_fma_f32 v[12:13], v[162:163], v[28:29], v[12:13] op_sel_hi:[0,1,1]
	v_pk_fma_f32 v[14:15], v[162:163], v[36:37], v[14:15] op_sel_hi:[0,1,1]
	v_pk_fma_f32 v[16:17], v[162:163], v[44:45], v[16:17] op_sel_hi:[0,1,1]
	v_fmac_f32_e32 v23, v162, v58
	v_pk_fma_f32 v[10:11], v[164:165], v[26:27], v[10:11] op_sel_hi:[0,1,1]
	v_pk_fma_f32 v[12:13], v[164:165], v[34:35], v[12:13] op_sel_hi:[0,1,1]
	v_pk_fma_f32 v[14:15], v[164:165], v[42:43], v[14:15] op_sel_hi:[0,1,1]
	v_pk_fma_f32 v[16:17], v[164:165], v[50:51], v[16:17] op_sel_hi:[0,1,1]
	v_fmac_f32_e32 v23, v164, v59
	ds_read_b128 v[24:27], v22 offset:4096
	ds_read_b128 v[28:31], v22 offset:8192
	ds_read_b128 v[32:35], v22 offset:12288
	ds_read_b128 v[36:39], v22 offset:16384
	ds_read_b128 v[40:43], v22 offset:20480
	ds_read_b128 v[44:47], v22 offset:24576
	ds_read_b128 v[48:51], v22 offset:28672
	ds_read_b128 v[52:55], v22
	ds_read_b128 v[56:59], v22 offset:32768
	s_waitcnt lgkmcnt(8)
	v_mov_b32_e32 v69, v24
	v_add_u32_e32 v22, 16, v22
	s_waitcnt lgkmcnt(1)
	v_mov_b32_e32 v68, v52
	v_mov_b32_e32 v24, v53
	v_mov_b32_e32 v52, v54
	v_mov_b32_e32 v53, v26
	v_mov_b32_e32 v26, v55
	v_mov_b32_e32 v54, v28
	v_mov_b32_e32 v55, v32
	v_mov_b32_e32 v32, v29
	v_mov_b32_e32 v28, v30
	v_mov_b32_e32 v29, v34
	v_mov_b32_e32 v34, v31
	v_mov_b32_e32 v30, v36
	v_mov_b32_e32 v31, v40
	v_mov_b32_e32 v40, v37
	v_mov_b32_e32 v36, v38
	v_mov_b32_e32 v37, v42
	v_mov_b32_e32 v42, v39
	v_mov_b32_e32 v38, v44
	v_mov_b32_e32 v39, v48
	v_mov_b32_e32 v48, v45
	v_mov_b32_e32 v44, v46
	v_mov_b32_e32 v45, v50
	v_mov_b32_e32 v50, v47
	s_waitcnt vmcnt(44)
	v_pk_fma_f32 v[10:11], v[166:167], v[68:69], v[10:11] op_sel_hi:[0,1,1]
	v_pk_fma_f32 v[12:13], v[166:167], v[54:55], v[12:13] op_sel_hi:[0,1,1]
	v_pk_fma_f32 v[14:15], v[166:167], v[30:31], v[14:15] op_sel_hi:[0,1,1]
	v_pk_fma_f32 v[16:17], v[166:167], v[38:39], v[16:17] op_sel_hi:[0,1,1]
	s_waitcnt lgkmcnt(0)
	v_fmac_f32_e32 v23, v166, v56
	v_pk_fma_f32 v[10:11], v[168:169], v[24:25], v[10:11] op_sel_hi:[0,1,1]
	v_pk_fma_f32 v[12:13], v[168:169], v[32:33], v[12:13] op_sel_hi:[0,1,1]
	v_pk_fma_f32 v[14:15], v[168:169], v[40:41], v[14:15] op_sel_hi:[0,1,1]
	v_pk_fma_f32 v[16:17], v[168:169], v[48:49], v[16:17] op_sel_hi:[0,1,1]
	v_fmac_f32_e32 v23, v168, v57
	v_pk_fma_f32 v[10:11], v[170:171], v[52:53], v[10:11] op_sel_hi:[0,1,1]
	v_pk_fma_f32 v[12:13], v[170:171], v[28:29], v[12:13] op_sel_hi:[0,1,1]
	v_pk_fma_f32 v[14:15], v[170:171], v[36:37], v[14:15] op_sel_hi:[0,1,1]
	v_pk_fma_f32 v[16:17], v[170:171], v[44:45], v[16:17] op_sel_hi:[0,1,1]
	v_fmac_f32_e32 v23, v170, v58
	v_pk_fma_f32 v[10:11], v[172:173], v[26:27], v[10:11] op_sel_hi:[0,1,1]
	v_pk_fma_f32 v[12:13], v[172:173], v[34:35], v[12:13] op_sel_hi:[0,1,1]
	v_pk_fma_f32 v[14:15], v[172:173], v[42:43], v[14:15] op_sel_hi:[0,1,1]
	v_pk_fma_f32 v[16:17], v[172:173], v[50:51], v[16:17] op_sel_hi:[0,1,1]
	v_fmac_f32_e32 v23, v172, v59
	ds_read_b128 v[24:27], v22 offset:4096
	ds_read_b128 v[28:31], v22 offset:8192
	ds_read_b128 v[32:35], v22 offset:12288
	ds_read_b128 v[36:39], v22 offset:16384
	ds_read_b128 v[40:43], v22 offset:20480
	ds_read_b128 v[44:47], v22 offset:24576
	ds_read_b128 v[48:51], v22 offset:28672
	ds_read_b128 v[52:55], v22
	ds_read_b128 v[56:59], v22 offset:32768
	s_waitcnt lgkmcnt(8)
	v_mov_b32_e32 v69, v24
	v_add_u32_e32 v22, 16, v22
	s_waitcnt lgkmcnt(1)
	v_mov_b32_e32 v68, v52
	v_mov_b32_e32 v24, v53
	v_mov_b32_e32 v52, v54
	v_mov_b32_e32 v53, v26
	v_mov_b32_e32 v26, v55
	v_mov_b32_e32 v54, v28
	v_mov_b32_e32 v55, v32
	v_mov_b32_e32 v32, v29
	v_mov_b32_e32 v28, v30
	v_mov_b32_e32 v29, v34
	v_mov_b32_e32 v34, v31
	v_mov_b32_e32 v30, v36
	v_mov_b32_e32 v31, v40
	v_mov_b32_e32 v40, v37
	v_mov_b32_e32 v36, v38
	v_mov_b32_e32 v37, v42
	v_mov_b32_e32 v42, v39
	v_mov_b32_e32 v38, v44
	v_mov_b32_e32 v39, v48
	v_mov_b32_e32 v48, v45
	v_mov_b32_e32 v44, v46
	v_mov_b32_e32 v45, v50
	v_mov_b32_e32 v50, v47
	s_waitcnt vmcnt(40)
	v_pk_fma_f32 v[10:11], v[174:175], v[68:69], v[10:11] op_sel_hi:[0,1,1]
	v_pk_fma_f32 v[12:13], v[174:175], v[54:55], v[12:13] op_sel_hi:[0,1,1]
	v_pk_fma_f32 v[14:15], v[174:175], v[30:31], v[14:15] op_sel_hi:[0,1,1]
	v_pk_fma_f32 v[16:17], v[174:175], v[38:39], v[16:17] op_sel_hi:[0,1,1]
	s_waitcnt lgkmcnt(0)
	v_fmac_f32_e32 v23, v174, v56
	v_pk_fma_f32 v[10:11], v[176:177], v[24:25], v[10:11] op_sel_hi:[0,1,1]
	v_pk_fma_f32 v[12:13], v[176:177], v[32:33], v[12:13] op_sel_hi:[0,1,1]
	v_pk_fma_f32 v[14:15], v[176:177], v[40:41], v[14:15] op_sel_hi:[0,1,1]
	v_pk_fma_f32 v[16:17], v[176:177], v[48:49], v[16:17] op_sel_hi:[0,1,1]
	v_fmac_f32_e32 v23, v176, v57
	v_pk_fma_f32 v[10:11], v[178:179], v[52:53], v[10:11] op_sel_hi:[0,1,1]
	v_pk_fma_f32 v[12:13], v[178:179], v[28:29], v[12:13] op_sel_hi:[0,1,1]
	v_pk_fma_f32 v[14:15], v[178:179], v[36:37], v[14:15] op_sel_hi:[0,1,1]
	v_pk_fma_f32 v[16:17], v[178:179], v[44:45], v[16:17] op_sel_hi:[0,1,1]
	v_fmac_f32_e32 v23, v178, v58
	v_pk_fma_f32 v[10:11], v[180:181], v[26:27], v[10:11] op_sel_hi:[0,1,1]
	v_pk_fma_f32 v[12:13], v[180:181], v[34:35], v[12:13] op_sel_hi:[0,1,1]
	v_pk_fma_f32 v[14:15], v[180:181], v[42:43], v[14:15] op_sel_hi:[0,1,1]
	v_pk_fma_f32 v[16:17], v[180:181], v[50:51], v[16:17] op_sel_hi:[0,1,1]
	v_fmac_f32_e32 v23, v180, v59
	ds_read_b128 v[24:27], v22 offset:4096
	ds_read_b128 v[28:31], v22 offset:8192
	ds_read_b128 v[32:35], v22 offset:12288
	ds_read_b128 v[36:39], v22 offset:16384
	ds_read_b128 v[40:43], v22 offset:20480
	ds_read_b128 v[44:47], v22 offset:24576
	ds_read_b128 v[48:51], v22 offset:28672
	ds_read_b128 v[52:55], v22
	ds_read_b128 v[56:59], v22 offset:32768
	s_waitcnt lgkmcnt(8)
	v_mov_b32_e32 v69, v24
	v_add_u32_e32 v22, 16, v22
	s_waitcnt lgkmcnt(1)
	v_mov_b32_e32 v68, v52
	v_mov_b32_e32 v24, v53
	v_mov_b32_e32 v52, v54
	v_mov_b32_e32 v53, v26
	v_mov_b32_e32 v26, v55
	v_mov_b32_e32 v54, v28
	v_mov_b32_e32 v55, v32
	v_mov_b32_e32 v32, v29
	v_mov_b32_e32 v28, v30
	v_mov_b32_e32 v29, v34
	v_mov_b32_e32 v34, v31
	v_mov_b32_e32 v30, v36
	v_mov_b32_e32 v31, v40
	v_mov_b32_e32 v40, v37
	v_mov_b32_e32 v36, v38
	v_mov_b32_e32 v37, v42
	v_mov_b32_e32 v42, v39
	v_mov_b32_e32 v38, v44
	v_mov_b32_e32 v39, v48
	v_mov_b32_e32 v48, v45
	v_mov_b32_e32 v44, v46
	v_mov_b32_e32 v45, v50
	v_mov_b32_e32 v50, v47
	s_waitcnt vmcnt(36)
	v_pk_fma_f32 v[10:11], v[182:183], v[68:69], v[10:11] op_sel_hi:[0,1,1]
	v_pk_fma_f32 v[12:13], v[182:183], v[54:55], v[12:13] op_sel_hi:[0,1,1]
	v_pk_fma_f32 v[14:15], v[182:183], v[30:31], v[14:15] op_sel_hi:[0,1,1]
	v_pk_fma_f32 v[16:17], v[182:183], v[38:39], v[16:17] op_sel_hi:[0,1,1]
	s_waitcnt lgkmcnt(0)
	v_fmac_f32_e32 v23, v182, v56
	v_pk_fma_f32 v[10:11], v[184:185], v[24:25], v[10:11] op_sel_hi:[0,1,1]
	v_pk_fma_f32 v[12:13], v[184:185], v[32:33], v[12:13] op_sel_hi:[0,1,1]
	v_pk_fma_f32 v[14:15], v[184:185], v[40:41], v[14:15] op_sel_hi:[0,1,1]
	v_pk_fma_f32 v[16:17], v[184:185], v[48:49], v[16:17] op_sel_hi:[0,1,1]
	v_fmac_f32_e32 v23, v184, v57
	v_pk_fma_f32 v[10:11], v[186:187], v[52:53], v[10:11] op_sel_hi:[0,1,1]
	v_pk_fma_f32 v[12:13], v[186:187], v[28:29], v[12:13] op_sel_hi:[0,1,1]
	v_pk_fma_f32 v[14:15], v[186:187], v[36:37], v[14:15] op_sel_hi:[0,1,1]
	v_pk_fma_f32 v[16:17], v[186:187], v[44:45], v[16:17] op_sel_hi:[0,1,1]
	v_fmac_f32_e32 v23, v186, v58
	v_pk_fma_f32 v[10:11], v[188:189], v[26:27], v[10:11] op_sel_hi:[0,1,1]
	v_pk_fma_f32 v[12:13], v[188:189], v[34:35], v[12:13] op_sel_hi:[0,1,1]
	v_pk_fma_f32 v[14:15], v[188:189], v[42:43], v[14:15] op_sel_hi:[0,1,1]
	v_pk_fma_f32 v[16:17], v[188:189], v[50:51], v[16:17] op_sel_hi:[0,1,1]
	v_fmac_f32_e32 v23, v188, v59
	ds_read_b128 v[24:27], v22 offset:4096
	ds_read_b128 v[28:31], v22 offset:8192
	ds_read_b128 v[32:35], v22 offset:12288
	ds_read_b128 v[36:39], v22 offset:16384
	ds_read_b128 v[40:43], v22 offset:20480
	ds_read_b128 v[44:47], v22 offset:24576
	ds_read_b128 v[48:51], v22 offset:28672
	ds_read_b128 v[52:55], v22
	ds_read_b128 v[56:59], v22 offset:32768
	s_waitcnt lgkmcnt(8)
	v_mov_b32_e32 v69, v24
	v_add_u32_e32 v22, 16, v22
	s_waitcnt lgkmcnt(1)
	v_mov_b32_e32 v68, v52
	v_mov_b32_e32 v24, v53
	v_mov_b32_e32 v52, v54
	v_mov_b32_e32 v53, v26
	v_mov_b32_e32 v26, v55
	v_mov_b32_e32 v54, v28
	v_mov_b32_e32 v55, v32
	v_mov_b32_e32 v32, v29
	v_mov_b32_e32 v28, v30
	v_mov_b32_e32 v29, v34
	v_mov_b32_e32 v34, v31
	v_mov_b32_e32 v30, v36
	v_mov_b32_e32 v31, v40
	v_mov_b32_e32 v40, v37
	v_mov_b32_e32 v36, v38
	v_mov_b32_e32 v37, v42
	v_mov_b32_e32 v42, v39
	v_mov_b32_e32 v38, v44
	v_mov_b32_e32 v39, v48
	v_mov_b32_e32 v48, v45
	v_mov_b32_e32 v44, v46
	v_mov_b32_e32 v45, v50
	v_mov_b32_e32 v50, v47
	s_waitcnt vmcnt(32)
	v_pk_fma_f32 v[10:11], v[190:191], v[68:69], v[10:11] op_sel_hi:[0,1,1]
	v_pk_fma_f32 v[12:13], v[190:191], v[54:55], v[12:13] op_sel_hi:[0,1,1]
	v_pk_fma_f32 v[14:15], v[190:191], v[30:31], v[14:15] op_sel_hi:[0,1,1]
	v_pk_fma_f32 v[16:17], v[190:191], v[38:39], v[16:17] op_sel_hi:[0,1,1]
	s_waitcnt lgkmcnt(0)
	v_fmac_f32_e32 v23, v190, v56
	v_pk_fma_f32 v[10:11], v[192:193], v[24:25], v[10:11] op_sel_hi:[0,1,1]
	v_pk_fma_f32 v[12:13], v[192:193], v[32:33], v[12:13] op_sel_hi:[0,1,1]
	v_pk_fma_f32 v[14:15], v[192:193], v[40:41], v[14:15] op_sel_hi:[0,1,1]
	v_pk_fma_f32 v[16:17], v[192:193], v[48:49], v[16:17] op_sel_hi:[0,1,1]
	v_fmac_f32_e32 v23, v192, v57
	v_pk_fma_f32 v[10:11], v[194:195], v[52:53], v[10:11] op_sel_hi:[0,1,1]
	v_pk_fma_f32 v[12:13], v[194:195], v[28:29], v[12:13] op_sel_hi:[0,1,1]
	v_pk_fma_f32 v[14:15], v[194:195], v[36:37], v[14:15] op_sel_hi:[0,1,1]
	v_pk_fma_f32 v[16:17], v[194:195], v[44:45], v[16:17] op_sel_hi:[0,1,1]
	v_fmac_f32_e32 v23, v194, v58
	v_pk_fma_f32 v[10:11], v[196:197], v[26:27], v[10:11] op_sel_hi:[0,1,1]
	v_pk_fma_f32 v[12:13], v[196:197], v[34:35], v[12:13] op_sel_hi:[0,1,1]
	v_pk_fma_f32 v[14:15], v[196:197], v[42:43], v[14:15] op_sel_hi:[0,1,1]
	v_pk_fma_f32 v[16:17], v[196:197], v[50:51], v[16:17] op_sel_hi:[0,1,1]
	v_fmac_f32_e32 v23, v196, v59
	s_add_i32 s6, s6, 1
	s_cmp_lt_u32 s6, 4
	s_cbranch_scc1 .Lada_loop
	ds_write2st64_b32 v20, v10, v11 offset0:144 offset1:146
	ds_write2st64_b32 v20, v12, v13 offset0:148 offset1:150
	ds_write2st64_b32 v20, v14, v15 offset0:152 offset1:154
	ds_write2st64_b32 v20, v16, v17 offset0:156 offset1:158
	ds_write_b32 v20, v23 offset:40960
	s_waitcnt lgkmcnt(0)
	s_barrier
	s_and_saveexec_b64 s[6:7], s[2:3]
	s_cbranch_execz .LBB0_14
	v_readlane_b32 s16, v251, 1
	s_mul_i32 s15, s4, 0x6000
	v_readlane_b32 s26, v251, 11
	s_mul_hi_i32 s5, s4, 0x6000
	v_readlane_b32 s17, v251, 2
	v_readlane_b32 s27, v251, 12
	s_add_u32 s16, s26, s15
	s_addc_u32 s17, s27, s5
	v_lshlrev_b64 v[6:7], 2, v[6:7]
	v_lshl_add_u64 v[8:9], s[16:17], 0, v[6:7]
	global_load_dword v60, v[8:9], off
	v_lshl_add_u64 v[6:7], s[0:1], 0, v[6:7]
	v_mad_i64_i32 v[6:7], s[4:5], s4, v21, v[6:7]
	v_add_co_u32_e32 v48, vcc, s8, v6
	ds_read2st64_b32 v[8:9], v1 offset0:144 offset1:146
	ds_read2st64_b32 v[10:11], v1 offset0:160 offset1:162
	ds_read2st64_b32 v[12:13], v1 offset0:180 offset1:182
	ds_read2st64_b32 v[14:15], v1 offset0:196 offset1:198
	ds_read2st64_b32 v[16:17], v1 offset0:164 offset1:166
	ds_read2st64_b32 v[22:23], v1 offset0:200 offset1:202
	ds_read2st64_b32 v[24:25], v1 offset0:148 offset1:150
	ds_read2st64_b32 v[26:27], v1 offset0:184 offset1:186
	ds_read2st64_b32 v[28:29], v1 offset0:168 offset1:170
	ds_read2st64_b32 v[30:31], v1 offset0:204 offset1:206
	ds_read2st64_b32 v[32:33], v1 offset0:152 offset1:154
	ds_read2st64_b32 v[34:35], v1 offset0:188 offset1:190
	ds_read2st64_b32 v[36:37], v1 offset0:172 offset1:174
	ds_read2st64_b32 v[38:39], v1 offset0:208 offset1:210
	ds_read2st64_b32 v[40:41], v1 offset0:156 offset1:158
	ds_read2st64_b32 v[42:43], v1 offset0:192 offset1:194
	ds_read2st64_b32 v[44:45], v1 offset0:176 offset1:178
	ds_read2st64_b32 v[46:47], v1 offset0:212 offset1:214
	v_addc_co_u32_e32 v49, vcc, 0, v7, vcc
	v_add_co_u32_e32 v50, vcc, s9, v6
	s_waitcnt lgkmcnt(14)
	v_add_f32_e32 v8, v8, v11
	v_addc_co_u32_e32 v51, vcc, 0, v7, vcc
	v_add_co_u32_e32 v52, vcc, s10, v6
	s_waitcnt lgkmcnt(13)
	v_add_f32_e32 v9, v9, v16
	v_addc_co_u32_e32 v53, vcc, 0, v7, vcc
	v_add_co_u32_e32 v54, vcc, s11, v6
	s_waitcnt lgkmcnt(11)
	v_add_f32_e32 v11, v24, v17
	s_waitcnt lgkmcnt(9)
	v_add_f32_e32 v16, v25, v28
	s_waitcnt lgkmcnt(7)
	v_add_f32_e32 v17, v32, v29
	s_waitcnt lgkmcnt(5)
	v_add_f32_e32 v24, v33, v36
	v_add_f32_e32 v8, v8, v12
	v_addc_co_u32_e32 v55, vcc, 0, v7, vcc
	v_add_f32_e32 v9, v9, v13
	v_add_f32_e32 v11, v11, v26
	v_add_f32_e32 v12, v16, v27
	v_add_f32_e32 v13, v17, v34
	v_add_f32_e32 v16, v24, v35
	v_add_f32_e32 v8, v8, v15
	v_add_co_u32_e32 v56, vcc, s12, v6
	v_add_f32_e32 v9, v9, v22
	v_add_f32_e32 v11, v11, v23
	v_add_f32_e32 v12, v12, v30
	v_add_f32_e32 v13, v13, v31
	s_waitcnt lgkmcnt(4)
	v_add_f32_e32 v15, v16, v38
	v_addc_co_u32_e32 v57, vcc, 0, v7, vcc
	v_add_co_u32_e32 v58, vcc, s13, v6
	s_waitcnt lgkmcnt(3)
	v_add_f32_e32 v25, v40, v37
	v_addc_co_u32_e32 v59, vcc, 0, v7, vcc
	s_waitcnt lgkmcnt(2)
	v_add_f32_e32 v17, v25, v42
	v_add_f32_e32 v16, v17, v39
	v_readlane_b32 s18, v251, 3
	v_readlane_b32 s19, v251, 4
	v_readlane_b32 s20, v251, 5
	v_readlane_b32 s21, v251, 6
	v_readlane_b32 s22, v251, 7
	v_readlane_b32 s23, v251, 8
	v_readlane_b32 s24, v251, 9
	v_readlane_b32 s25, v251, 10
	v_readlane_b32 s28, v251, 13
	v_readlane_b32 s29, v251, 14
	v_readlane_b32 s30, v251, 15
	v_readlane_b32 s31, v251, 16
	s_waitcnt vmcnt(0)
	v_add_f32_e32 v8, v60, v8
	v_add_f32_e32 v9, v60, v9
	v_add_f32_e32 v11, v60, v11
	v_add_f32_e32 v12, v60, v12
	v_add_f32_e32 v13, v60, v13
	v_add_f32_e32 v15, v60, v15
	global_store_dword v[6:7], v8, off
	global_store_dword v[48:49], v9, off
	global_store_dword v[50:51], v11, off
	global_store_dword v[52:53], v12, off
	global_store_dword v[54:55], v13, off
	global_store_dword v[56:57], v15, off
	s_waitcnt lgkmcnt(1)
	v_add_f32_e32 v8, v41, v44
	v_add_f32_e32 v8, v8, v43
	s_waitcnt lgkmcnt(0)
	v_add_f32_e32 v8, v8, v46
	v_add_f32_e32 v11, v60, v8
	v_add_co_u32_e32 v8, vcc, 0x2a000, v6
	v_add_f32_e32 v16, v60, v16
	s_nop 0
	v_addc_co_u32_e32 v9, vcc, 0, v7, vcc
	global_store_dword v[8:9], v11, off
	v_add_f32_e32 v8, v10, v45
	v_add_f32_e32 v8, v8, v14
	v_add_f32_e32 v8, v8, v47
	v_add_co_u32_e32 v6, vcc, 0x30000, v6
	v_add_f32_e32 v8, v60, v8
	s_nop 0
	v_addc_co_u32_e32 v7, vcc, 0, v7, vcc
	global_store_dword v[58:59], v16, off
	global_store_dword v[6:7], v8, off
	s_branch .LBB0_14

.LBB0_818:
	s_or_b64 exec, exec, s[30:31]
	v_readlane_b32 s0, v255, 32
	v_mov_b32_e32 v2, v0
	s_waitcnt lgkmcnt(0)
	s_barrier
	v_readlane_b32 s1, v255, 33
	s_mov_b32 s1, s79
	v_ashrrev_i32_e32 v10, 6, v2
	v_readlane_b32 s4, v251, 19
	v_add_u32_e32 v10, s89, v10
	s_lshl_b32 s78, s0, 7
	v_writelane_b32 v255, s0, 6
	v_readlane_b32 s5, v251, 20
	v_lshl_add_u32 v90, v10, 3, v10
	v_writelane_b32 v255, s1, 7
	s_lshl_b64 s[0:1], s[78:79], 2
	v_readlane_b32 s12, v251, 27
	v_lshlrev_b32_e32 v12, 3, v2
	v_ashrrev_i32_e32 v91, 31, v90
	v_readlane_b32 s4, v252, 53
	v_readlane_b32 s13, v251, 28
	s_add_u32 s0, s12, s0
	v_lshlrev_b32_e32 v2, 5, v2
	v_lshlrev_b64 v[10:11], 10, v[90:91]
	v_readlane_b32 s5, v252, 54
	v_and_b32_e32 v92, 0x1f8, v12
	s_addc_u32 s1, s13, s1
	v_and_b32_e32 v6, 0x1e0, v2
	v_lshl_add_u64 v[10:11], s[4:5], 0, v[10:11]
	v_lshlrev_b32_e32 v130, 1, v92
	global_load_dwordx4 v[2:5], v6, s[0:1] offset:16
	s_nop 0
	global_load_dwordx4 v[6:9], v6, s[0:1]
	v_lshl_add_u64 v[10:11], v[10:11], 0, v[130:131]
	s_mov_b32 s0, 0x1200000
	v_add_co_u32_e32 v12, vcc, s0, v10
	v_readlane_b32 s7, v251, 22
	s_nop 0
	v_addc_co_u32_e32 v13, vcc, 0, v11, vcc
	global_load_dwordx4 v[86:89], v[10:11], off nt
	global_load_dwordx4 v[82:85], v[12:13], off nt
	v_mov_b64_e32 v[10:11], s[92:93]
	v_mad_i64_i32 v[10:11], s[0:1], v90, s81, v[10:11]
	v_lshl_add_u64 v[10:11], v[10:11], 0, v[130:131]
	s_mov_b32 s0, 0x6cdc000
	v_add_co_u32_e32 v12, vcc, s0, v10
	s_mov_b32 s0, 0x6cdd000
	s_nop 0
	v_addc_co_u32_e32 v13, vcc, 0, v11, vcc
	v_add_co_u32_e32 v10, vcc, s0, v10
	v_readlane_b32 s2, v252, 23
	s_nop 0
	v_addc_co_u32_e32 v11, vcc, 0, v11, vcc
	global_load_dwordx4 v[78:81], v[12:13], off offset:512 nt
	global_load_dwordx4 v[18:21], v[10:11], off offset:32 nt
	v_lshlrev_b64 v[10:11], 11, v[90:91]
	v_lshlrev_b32_e32 v12, 2, v92
	v_or_b32_e32 v10, v10, v12
	v_readlane_b32 s3, v252, 24
	v_lshl_add_u64 v[16:17], s[92:93], 0, v[10:11]
	s_mov_b32 s7, 0x28d5d000
	s_mov_b64 s[0:1], 0x2400000
	v_lshl_add_u64 v[14:15], s[2:3], 0, v[10:11]
	v_add_co_u32_e32 v16, vcc, s7, v16
	v_lshl_add_u64 v[10:11], v[10:11], 0, s[0:1]
	s_nop 0
	v_addc_co_u32_e32 v17, vcc, 0, v17, vcc
	global_load_dwordx4 v[58:61], v[14:15], off nt
	global_load_dwordx4 v[30:33], v[16:17], off offset:2832 nt
	v_lshl_add_u64 v[14:15], s[2:3], 0, v[10:11]
	v_lshl_add_u64 v[10:11], s[92:93], 0, v[10:11]
	v_add_co_u32_e32 v10, vcc, s7, v10
	v_readlane_b32 s0, v254, 22
	s_nop 0
	v_addc_co_u32_e32 v11, vcc, 0, v11, vcc
	global_load_dwordx4 v[66:69], v[14:15], off nt
	global_load_dwordx4 v[34:37], v[10:11], off offset:2832 nt
	v_readlane_b32 s1, v254, 23
	v_readlane_b32 s6, v251, 21
	v_mov_b32_e32 v13, v131
	v_lshl_add_u64 v[98:99], s[0:1], 0, v[130:131]
	v_readlane_b32 s0, v252, 34
	v_readlane_b32 s1, v252, 35
	v_mov_b32_e32 v10, 0
	s_mov_b32 s6, 0x28d5d000
	s_mov_b32 s2, 0
	v_or_b32_e32 v94, 0x900000, v92
	v_mov_b32_e32 v95, v131
	v_lshl_add_u64 v[96:97], s[4:5], 0, v[130:131]
	v_lshl_add_u64 v[100:101], s[0:1], 0, v[12:13]
	v_mov_b32_e32 v91, -1
	v_lshlrev_b32_e32 v130, 1, v92
	v_mov_b32_e32 v11, v10
	v_mov_b32_e32 v12, v10
	v_mov_b32_e32 v13, v10
	v_mov_b32_e32 v14, v10
	v_mov_b32_e32 v15, v10
	v_mov_b32_e32 v16, v10
	v_mov_b32_e32 v17, v10
	v_mov_b32_e32 v22, v10
	v_mov_b32_e32 v23, v10
	v_mov_b32_e32 v24, v10
	v_mov_b32_e32 v25, v10
	v_mov_b32_e32 v26, v10
	v_mov_b32_e32 v27, v10
	v_mov_b32_e32 v28, v10
	v_mov_b32_e32 v29, v10
	s_mov_b64 s[78:79], 0x40000
	v_readlane_b32 s8, v251, 23
	v_readlane_b32 s9, v251, 24
	v_readlane_b32 s10, v251, 25
	v_readlane_b32 s11, v251, 26
	v_readlane_b32 s14, v251, 29
	v_readlane_b32 s15, v251, 30
	v_readlane_b32 s16, v251, 31
	v_readlane_b32 s17, v251, 32
	v_readlane_b32 s18, v251, 33
	v_readlane_b32 s19, v251, 34
	s_branch .LBB0_820

.LBB0_820:
	v_add_u32_e32 v93, s2, v90
	s_movk_i32 s0, 0x3fff
	v_cmp_lt_i32_e32 vcc, s0, v93
	s_and_saveexec_b64 s[0:1], vcc
	s_xor_b64 s[0:1], exec, s[0:1]
	v_add_u32_e32 v38, 0xffffc000, v93
	v_lshrrev_b32_e32 v38, 6, v38
	v_add_u32_e32 v102, 0x100, v38
	s_andn2_saveexec_b64 s[0:1], s[0:1]
	v_ashrrev_i32_e32 v38, 31, v93
	v_lshrrev_b32_e32 v38, 26, v38
	v_add_u32_e32 v38, v93, v38
	v_ashrrev_i32_e32 v102, 6, v38
	s_or_b64 exec, exec, s[0:1]
	s_cmp_lg_u32 s2, 8
	s_cselect_b64 vcc, -1, 0
	v_addc_co_u32_e32 v54, vcc, 0, v93, vcc
	v_ashrrev_i32_e32 v55, 31, v54
	v_lshlrev_b64 v[38:39], 10, v[54:55]
	v_lshl_add_u64 v[38:39], v[96:97], 0, v[38:39]
	v_mov_b64_e32 v[46:47], s[92:93]
	v_add_co_u32_e32 v42, vcc, 0x1200000, v38
	v_mad_i64_i32 v[46:47], s[0:1], v54, s81, v[46:47]
	s_nop 0
	v_addc_co_u32_e32 v43, vcc, 0, v39, vcc
	v_lshl_add_u64 v[46:47], v[46:47], 0, v[130:131]
	s_mov_b32 s0, 0x6cdc000
	v_add_co_u32_e32 v48, vcc, s0, v46
	s_mov_b32 s0, 0x6cdd000
	s_nop 0
	v_addc_co_u32_e32 v49, vcc, 0, v47, vcc
	v_lshlrev_b64 v[70:71], 9, v[54:55]
	v_add_co_u32_e32 v50, vcc, s0, v46
	v_or_b32_e32 v54, v70, v92
	v_mov_b32_e32 v55, v71
	v_readlane_b32 s0, v252, 23
	v_lshlrev_b64 v[54:55], 2, v[54:55]
	v_readlane_b32 s1, v252, 24
	v_addc_co_u32_e32 v51, vcc, 0, v47, vcc
	s_nop 0
	v_lshl_add_u64 v[56:57], s[0:1], 0, v[54:55]
	v_lshl_add_u64 v[54:55], s[92:93], 0, v[54:55]
	v_lshl_add_u64 v[70:71], v[70:71], 0, v[94:95]
	v_add_co_u32_e32 v62, vcc, s6, v54
	v_lshlrev_b64 v[70:71], 2, v[70:71]
	s_nop 0
	v_addc_co_u32_e32 v63, vcc, 0, v55, vcc
	v_lshl_add_u64 v[72:73], s[0:1], 0, v[70:71]
	v_lshl_add_u64 v[70:71], s[92:93], 0, v[70:71]
	v_add_co_u32_e32 v74, vcc, 0x28d5d000, v70
	global_load_dwordx4 v[38:41], v[38:39], off nt
	s_nop 0
	global_load_dwordx4 v[42:45], v[42:43], off nt
	v_addc_co_u32_e32 v75, vcc, 0, v71, vcc
	global_load_dwordx4 v[46:49], v[48:49], off offset:512 nt
	s_nop 0
	global_load_dwordx4 v[50:53], v[50:51], off offset:32 nt
	s_nop 0
	global_load_dwordx4 v[54:57], v[56:57], off nt
	s_nop 0
	global_load_dwordx4 v[62:65], v[62:63], off offset:2832 nt
	s_nop 0
	global_load_dwordx4 v[70:73], v[72:73], off nt
	s_nop 0
	global_load_dwordx4 v[74:77], v[74:75], off offset:2832 nt
	v_cmp_ne_u32_e32 vcc, v102, v91
	s_and_saveexec_b64 s[0:1], vcc
	s_cbranch_execz .LBB0_819
	v_ashrrev_i32_e32 v103, 31, v102
	v_lshlrev_b64 v[10:11], 11, v[102:103]
	v_lshl_add_u64 v[22:23], v[100:101], 0, v[10:11]
	s_mov_b64 s[4:5], 0x90000
	global_load_dwordx4 v[14:17], v[22:23], off offset:16 nt
	global_load_dwordx4 v[10:13], v[22:23], off nt
	v_lshl_add_u64 v[26:27], v[22:23], 0, s[4:5]
	v_add_co_u32_e32 v22, vcc, 0x90000, v22
	v_mov_b32_e32 v91, v102
	s_nop 0
	v_addc_co_u32_e32 v23, vcc, 0, v23, vcc
	global_load_dwordx4 v[22:25], v[22:23], off nt
	s_nop 0
	global_load_dwordx4 v[26:29], v[26:27], off offset:16 nt
	s_waitcnt vmcnt(0)
	s_branch .LBB0_819
